# baseline (speedup 1.0000x reference)
_Z15k_scatter_gemm1PKiS0_PiPjPyPKfPK6__halfS5_S5_PS6_PfSA_:
	s_cmpk_gt_u32 s2, 0x186
	s_mov_b64 s[4:5], -1
	s_cbranch_scc0 .LBB1_22
	s_load_dwordx2 s[26:27], s[0:1], 0x28
	s_load_dwordx2 s[10:11], s[0:1], 0x30
	s_load_dwordx4 s[28:31], s[0:1], 0x38
	v_lshlrev_b32_e32 v92, 4, v0
	v_add_u32_e32 v93, 0x1000, v92
	v_add_u32_e32 v94, 0x2000, v92
	v_add_u32_e32 v95, 0x3000, v92
	v_add_u32_e32 v96, 0x4000, v92
	v_add_u32_e32 v97, 0x5000, v92
	v_add_u32_e32 v98, 0x6000, v92
	v_add_u32_e32 v99, 0x7000, v92
	v_add_u32_e32 v100, 0x8000, v92
	v_lshlrev_b32_e32 v101, 2, v0
	s_movk_i32 s3, 0x80
	v_cmp_gt_u32_e64 s[8:9], s3, v0
	s_mov_b32 s40, 0xbc8000
	s_mov_b32 s41, 0
	s_mov_b32 s42, 1
	s_waitcnt lgkmcnt(0)
	global_load_dwordx4 v[50:53], v92, s[10:11]
	global_load_dwordx4 v[54:57], v93, s[10:11]
	global_load_dwordx4 v[58:61], v94, s[10:11]
	global_load_dwordx4 v[62:65], v95, s[10:11]
	global_load_dwordx4 v[68:71], v96, s[10:11]
	global_load_dwordx4 v[72:75], v97, s[10:11]
	global_load_dwordx4 v[76:79], v98, s[10:11]
	global_load_dwordx4 v[84:87], v99, s[10:11]
	s_and_saveexec_b64 s[4:5], s[8:9]
	global_load_dwordx4 v[88:91], v100, s[10:11]
	global_load_dword v102, v101, s[28:29]
	global_load_dword v103, v101, s[30:31]
	s_mov_b64 exec, s[4:5]
	s_lshl_b32 s3, s2, 2
	v_lshrrev_b32_e32 v14, 6, v0
	s_add_i32 s4, s3, 0xfffff9e4
	v_or_b32_e32 v2, s4, v14
	s_movk_i32 s4, 2500
	v_cmp_gt_i32_e32 vcc, s4, v2
	v_and_b32_e32 v1, 15, v0
	v_and_b32_e32 v66, 48, v0
	v_mov_b32_e32 v67, 0
	s_movk_i32 s43, 992
	v_cmp_gt_i32_e64 s[38:39], s43, v2
	s_and_saveexec_b64 s[6:7], vcc
	s_cbranch_execz .Lg1_noval
	v_lshl_or_b32 v2, v2, 4, v1
	v_ashrrev_i32_e32 v3, 31, v2
	v_lshlrev_b64 v[2:3], 9, v[2:3]
	v_lshl_add_u64 v[2:3], s[26:27], 0, v[2:3]
	v_lshl_add_u64 v[16:17], v[2:3], 0, v[66:67]
	global_load_dwordx4 v[38:41], v[16:17], off offset:448
	global_load_dwordx4 v[34:37], v[16:17], off offset:384
	global_load_dwordx4 v[46:49], v[16:17], off offset:320
	global_load_dwordx4 v[42:45], v[16:17], off offset:256
	global_load_dwordx4 v[6:9], v[16:17], off offset:192
	global_load_dwordx4 v[18:21], v[16:17], off offset:128
	global_load_dwordx4 v[2:5], v[16:17], off offset:64
	global_load_dwordx4 v[10:13], v[16:17], off
	s_cmp_eq_u64 s[38:39], 0
	s_cbranch_scc1 .Lg1_noB
	v_lshl_add_u64 v[16:17], v[16:17], 0, s[40:41]
	global_load_dwordx4 v[146:149], v[16:17], off
	global_load_dwordx4 v[150:153], v[16:17], off offset:64
	global_load_dwordx4 v[154:157], v[16:17], off offset:128
	global_load_dwordx4 v[158:161], v[16:17], off offset:192
	global_load_dwordx4 v[128:131], v[16:17], off offset:256
	global_load_dwordx4 v[132:135], v[16:17], off offset:320
	global_load_dwordx4 v[136:139], v[16:17], off offset:384
	global_load_dwordx4 v[140:143], v[16:17], off offset:448
	s_mov_b64 exec, s[6:7]
	s_waitcnt vmcnt(16)
	s_branch .Lg1_stage
.Lg1_noB:
	s_mov_b64 exec, s[6:7]
	s_waitcnt vmcnt(8)
	s_branch .Lg1_stage
.Lg1_noval:
	s_mov_b64 exec, s[6:7]
	s_mov_b64 s[38:39], 0
	s_waitcnt vmcnt(0)
.Lg1_stage:
	ds_write_b128 v92, v[50:53]
	ds_write_b128 v92, v[54:57] offset:4096
	ds_write_b128 v92, v[58:61] offset:8192
	ds_write_b128 v92, v[62:65] offset:12288
	ds_write_b128 v92, v[68:71] offset:16384
	ds_write_b128 v92, v[72:75] offset:20480
	ds_write_b128 v92, v[76:79] offset:24576
	ds_write_b128 v92, v[84:87] offset:28672
	s_and_saveexec_b64 s[4:5], s[8:9]
	ds_write_b128 v92, v[88:91] offset:32768
	ds_write2st64_b32 v101, v102, v103 offset0:204 offset1:206
	s_mov_b64 exec, s[4:5]
	s_waitcnt lgkmcnt(0)
	s_barrier
	s_and_saveexec_b64 s[6:7], vcc
	s_cbranch_execz .LBB1_21
	s_load_dwordx2 s[8:9], s[0:1], 0x58
	s_load_dwordx2 s[10:11], s[0:1], 0x48
	v_and_b32_e32 v15, 63, v0
	v_lshl_add_u64 v[68:69], s[26:27], 0, v[66:67]
	s_movk_i32 s4, 0x1100
	v_cmp_gt_u32_e32 vcc, 16, v15
	v_mul_u32_u24_e32 v15, 0x110, v1
	v_mul_u32_u24_e32 v17, 0x1100, v14
	v_mad_u32_u24 v22, v14, s4, v15
	v_lshlrev_b32_e32 v16, 4, v1
	v_add_u32_e32 v25, s3, v14
	v_lshlrev_b32_e32 v14, 4, v14
	v_bfe_u32 v80, v0, 4, 2
	v_or_b32_e32 v24, v17, v16
	v_mov_b32_e32 v17, v67
	v_lshl_or_b32 v82, s2, 6, v14
	v_mbcnt_lo_u32_b32 v14, -1, 0
	s_waitcnt lgkmcnt(0)
	v_lshl_add_u64 v[70:71], s[10:11], 0, v[16:17]
	v_or_b32_e32 v17, 4, v80
	v_mbcnt_hi_u32_b32 v84, -1, v14
	v_lshlrev_b32_e32 v23, 3, v80
	v_mul_u32_u24_e32 v16, 0x110, v80
	v_mul_u32_u24_e32 v17, 0x110, v17
	v_and_b32_e32 v14, 64, v84
	v_subrev_u32_e32 v67, 56, v25
	v_or_b32_e32 v81, 0xffff9e40, v1
	s_mov_b64 s[10:11], 0
	s_movk_i32 s3, 992
	v_add_u32_e32 v83, v66, v15
	v_xor_b32_e32 v85, 16, v84
	v_add_u32_e32 v86, 64, v14
	v_xor_b32_e32 v87, 32, v84
	v_add_u32_e32 v88, v22, v23
	v_add_u32_e32 v89, v24, v16
	v_add_u32_e32 v90, v24, v17
	s_movk_i32 s12, 991
	s_cmp_eq_u64 s[38:39], 0
	s_cbranch_scc1 .Lg1_w0
	s_waitcnt vmcnt(8)
	s_branch .LBB1_19
.Lg1_w0:
	s_waitcnt vmcnt(0)
	s_branch .LBB1_19
.LBB1_18:
	s_or_b64 exec, exec, s[4:5]
	v_cvt_pk_f16_f32 v41, v40, v41
	v_cvt_pk_f16_f32 v40, v38, v39
	v_cvt_pk_f16_f32 v38, v62, v63
	v_add_u32_e32 v62, 0x8800, v88
	v_cvt_pk_f16_f32 v37, v36, v37
	v_cvt_pk_f16_f32 v36, v34, v35
	v_cvt_pk_f16_f32 v35, v56, v57
	v_cvt_pk_f16_f32 v34, v54, v55
	ds_write2_b64 v62, v[36:37], v[34:35] offset0:8 offset1:12
	v_cvt_pk_f16_f32 v35, v44, v45
	v_cvt_pk_f16_f32 v34, v42, v43
	v_cvt_pk_f16_f32 v37, v48, v49
	v_cvt_pk_f16_f32 v36, v46, v47
	v_cvt_pk_f16_f32 v39, v64, v65
	ds_write2_b64 v62, v[34:35], v[36:37] offset0:16 offset1:20
	v_cvt_pk_f16_f32 v35, v52, v53
	v_cvt_pk_f16_f32 v34, v50, v51
	v_cvt_pk_f16_f32 v37, v60, v61
	v_cvt_pk_f16_f32 v36, v58, v59
	ds_write2_b64 v62, v[40:41], v[38:39] offset1:4
	ds_write2_b64 v62, v[34:35], v[36:37] offset0:24 offset1:28
	ds_read_b128 v[34:37], v89 offset:34816
	v_add_u32_e32 v44, v80, v82
	v_add_u32_e32 v38, 0xffff9e40, v44
	v_ashrrev_i32_e32 v39, 31, v38
	v_lshlrev_b64 v[38:39], 8, v[38:39]
	v_lshl_add_u64 v[42:43], v[70:71], 0, v[38:39]
	ds_read_b128 v[38:41], v90 offset:34816
	s_waitcnt lgkmcnt(1)
	global_store_dwordx4 v[42:43], v[34:37], off
	v_cmp_lt_i32_e64 s[4:5], s12, v91
	v_add_u32_e32 v67, 0x5e4, v67
	v_add_u32_e32 v34, 0xffff9e44, v44
	v_ashrrev_i32_e32 v35, 31, v34
	v_lshlrev_b64 v[34:35], 8, v[34:35]
	v_lshl_add_u64 v[34:35], v[70:71], 0, v[34:35]
	s_waitcnt lgkmcnt(0)
	global_store_dwordx4 v[34:35], v[38:41], off
	ds_read_b128 v[34:37], v90 offset:35904
	v_add_u32_e32 v82, 0x5e40, v82
	v_add_u32_e32 v38, 0xffff9e48, v44
	v_ashrrev_i32_e32 v39, 31, v38
	v_lshlrev_b64 v[38:39], 8, v[38:39]
	v_lshl_add_u64 v[42:43], v[70:71], 0, v[38:39]
	ds_read_b128 v[38:41], v90 offset:36992
	s_waitcnt lgkmcnt(1)
	global_store_dwordx4 v[42:43], v[34:37], off
	s_or_b64 s[10:11], s[4:5], s[10:11]
	s_waitcnt vmcnt(6)
	v_mov_b64_e32 v[42:43], v[26:27]
	v_add_u32_e32 v34, 0xffff9e4c, v44
	v_ashrrev_i32_e32 v35, 31, v34
	v_lshlrev_b64 v[34:35], 8, v[34:35]
	v_lshl_add_u64 v[34:35], v[70:71], 0, v[34:35]
	s_waitcnt lgkmcnt(0)
	global_store_dwordx4 v[34:35], v[38:41], off
	s_waitcnt vmcnt(5)
	v_mov_b64_e32 v[36:37], v[32:33]
	v_mov_b64_e32 v[34:35], v[30:31]
	v_mov_b64_e32 v[44:45], v[28:29]
	s_waitcnt vmcnt(4)
	v_mov_b64_e32 v[40:41], v[24:25]
	v_mov_b64_e32 v[38:39], v[22:23]
	v_mov_b64_e32 v[48:49], v[16:17]
	v_mov_b64_e32 v[46:47], v[14:15]
	s_mov_b32 s42, 0
	s_andn2_b64 exec, exec, s[10:11]
	s_cbranch_execz .LBB1_21
.LBB1_19:
	ds_read_b128 v[14:17], v83
	v_cvt_pk_f16_f32 v5, v4, v5
	v_cvt_pk_f16_f32 v4, v2, v3
	v_cvt_pk_f16_f32 v3, v12, v13
	v_cvt_pk_f16_f32 v2, v10, v11
	ds_read_b128 v[10:13], v83 offset:64
	ds_read_b128 v[22:25], v83 offset:4352
	ds_read_b128 v[26:29], v83 offset:4416
	ds_read_b128 v[30:33], v83 offset:8704
	ds_read_b128 v[50:53], v83 offset:8768
	ds_read_b128 v[54:57], v83 offset:13056
	ds_read_b128 v[58:61], v83 offset:13120
	ds_read_b128 v[62:65], v83 offset:17408
	ds_read_b128 v[72:75], v83 offset:17472
	ds_read_b128 v[76:79], v83 offset:21760
	ds_read_b128 v[92:95], v83 offset:21824
	ds_read_b128 v[96:99], v83 offset:26112
	ds_read_b128 v[100:103], v83 offset:26176
	ds_read_b128 v[104:107], v83 offset:30464
	ds_read_b128 v[110:113], v83 offset:30528
	v_add_u32_e32 v91, 0xfffffa1c, v67
	v_cmp_gt_i32_e64 s[4:5], s3, v91
	s_mov_b64 s[36:37], s[4:5]
	s_waitcnt lgkmcnt(14)
	v_mfma_f32_16x16x32_f16 v[14:17], v[14:17], v[2:5], 0
	v_cvt_pk_f16_f32 v109, v8, v9
	v_cvt_pk_f16_f32 v108, v6, v7
	v_cvt_pk_f16_f32 v49, v48, v49
	s_waitcnt lgkmcnt(13)
	v_mfma_f32_16x16x32_f16 v[22:25], v[22:25], v[2:5], 0
	v_cvt_pk_f16_f32 v48, v46, v47
	v_cvt_pk_f16_f32 v47, v44, v45
	v_cvt_pk_f16_f32 v46, v42, v43
	s_waitcnt lgkmcnt(11)
	v_mfma_f32_16x16x32_f16 v[30:33], v[30:33], v[2:5], 0
	s_waitcnt lgkmcnt(9)
	v_mfma_f32_16x16x32_f16 v[54:57], v[54:57], v[2:5], 0
	s_waitcnt lgkmcnt(7)
	v_mfma_f32_16x16x32_f16 v[62:65], v[62:65], v[2:5], 0
	s_waitcnt lgkmcnt(5)
	v_mfma_f32_16x16x32_f16 v[76:79], v[76:79], v[2:5], 0
	s_waitcnt lgkmcnt(3)
	v_mfma_f32_16x16x32_f16 v[96:99], v[96:99], v[2:5], 0
	s_waitcnt lgkmcnt(1)
	v_mfma_f32_16x16x32_f16 v[114:117], v[104:107], v[2:5], 0
	v_cndmask_b32_e64 v2, v91, v67, s[4:5]
	v_lshl_or_b32 v2, v2, 4, v1
	v_ashrrev_i32_e32 v3, 31, v2
	v_cvt_pk_f16_f32 v107, v20, v21
	v_cvt_pk_f16_f32 v106, v18, v19
	v_lshlrev_b64 v[2:3], 9, v[2:3]
	v_cmp_lt_i32_e64 s[4:5], v85, v86
	v_mfma_f32_16x16x32_f16 v[122:125], v[26:29], v[106:109], v[22:25]
	s_nop 2
	v_lshl_add_u64 v[22:23], v[68:69], 0, v[2:3]
	v_mfma_f32_16x16x32_f16 v[118:121], v[10:13], v[106:109], v[14:17]
	s_cmp_eq_u64 s[36:37], 0
	s_cbranch_scc1 .Lg1_nopfA
	s_cmp_lg_u32 s42, 0
	s_cbranch_scc1 .Lg1_firstA
	global_load_dwordx4 v[10:13], v[22:23], off
	global_load_dwordx4 v[2:5], v[22:23], off offset:64
	global_load_dwordx4 v[18:21], v[22:23], off offset:128
	global_load_dwordx4 v[6:9], v[22:23], off offset:192
	global_load_dwordx4 v[26:29], v[22:23], off offset:256
	global_load_dwordx4 v[14:17], v[22:23], off offset:320
	s_branch .Lg1_nopfA
.Lg1_firstA:
	s_waitcnt vmcnt(0)
	v_mov_b64_e32 v[10:11], v[146:147]
	v_mov_b64_e32 v[12:13], v[148:149]
	v_mov_b64_e32 v[2:3], v[150:151]
	v_mov_b64_e32 v[4:5], v[152:153]
	v_mov_b64_e32 v[18:19], v[154:155]
	v_mov_b64_e32 v[20:21], v[156:157]
	v_mov_b64_e32 v[6:7], v[158:159]
	v_mov_b64_e32 v[8:9], v[160:161]
	v_mov_b64_e32 v[26:27], v[128:129]
	v_mov_b64_e32 v[28:29], v[130:131]
	v_mov_b64_e32 v[14:15], v[132:133]
	v_mov_b64_e32 v[16:17], v[134:135]
.Lg1_nopfA:
	v_mfma_f32_16x16x32_f16 v[50:53], v[50:53], v[106:109], v[30:33]
	s_nop 2
	s_cmp_eq_u64 s[36:37], 0
	s_cbranch_scc1 .Lg1_nopfB
	s_cmp_lg_u32 s42, 0
	s_cbranch_scc1 .Lg1_firstB
	global_load_dwordx4 v[30:33], v[22:23], off offset:384
	s_nop 0
	global_load_dwordx4 v[22:25], v[22:23], off offset:448
	s_branch .Lg1_nopfB
.Lg1_firstB:
	v_mov_b64_e32 v[30:31], v[136:137]
	v_mov_b64_e32 v[32:33], v[138:139]
	v_mov_b64_e32 v[22:23], v[140:141]
	v_mov_b64_e32 v[24:25], v[142:143]

	.amdhsa_kernel _Z15k_scatter_gemm1PKiS0_PiPjPyPKfPK6__halfS5_S5_PS6_PfSA_
		.amdhsa_group_segment_fixed_size 53248
		.amdhsa_private_segment_fixed_size 0
		.amdhsa_kernarg_size 96
		.amdhsa_user_sgpr_count 2
		.amdhsa_user_sgpr_dispatch_ptr 0
		.amdhsa_user_sgpr_queue_ptr 0
		.amdhsa_user_sgpr_kernarg_segment_ptr 1
		.amdhsa_user_sgpr_dispatch_id 0
		.amdhsa_user_sgpr_kernarg_preload_length 0
		.amdhsa_user_sgpr_kernarg_preload_offset 0
		.amdhsa_user_sgpr_private_segment_size 0
		.amdhsa_uses_dynamic_stack 0
		.amdhsa_enable_private_segment 0
		.amdhsa_system_sgpr_workgroup_id_x 1
		.amdhsa_system_sgpr_workgroup_id_y 0
		.amdhsa_system_sgpr_workgroup_id_z 0
		.amdhsa_system_sgpr_workgroup_info 0
		.amdhsa_system_vgpr_workitem_id 0
		.amdhsa_next_free_vgpr 162
		.amdhsa_next_free_sgpr 96
		.amdhsa_accum_offset 164
		.amdhsa_reserve_vcc 1
		.amdhsa_float_round_mode_32 0
		.amdhsa_float_round_mode_16_64 0
		.amdhsa_float_denorm_mode_32 3
		.amdhsa_float_denorm_mode_16_64 3
		.amdhsa_dx10_clamp 1
		.amdhsa_ieee_mode 1
		.amdhsa_fp16_overflow 0
		.amdhsa_tg_split 0
		.amdhsa_exception_fp_ieee_invalid_op 0
		.amdhsa_exception_fp_denorm_src 0
		.amdhsa_exception_fp_ieee_div_zero 0
		.amdhsa_exception_fp_ieee_overflow 0
		.amdhsa_exception_fp_ieee_underflow 0
		.amdhsa_exception_fp_ieee_inexact 0
		.amdhsa_exception_int_div_zero 0
	.end_amdhsa_kernel

amdhsa.kernels:
  - .agpr_count:     0
    .args:
      - .actual_access:  read_only
        .address_space:  global
        .offset:         0
        .size:           8
        .value_kind:     global_buffer
      - .actual_access:  read_only
        .address_space:  global
        .offset:         8
        .size:           8
        .value_kind:     global_buffer
      - .actual_access:  write_only
        .address_space:  global
        .offset:         16
        .size:           8
        .value_kind:     global_buffer
      - .actual_access:  write_only
        .address_space:  global
        .offset:         24
        .size:           8
        .value_kind:     global_buffer
      - .actual_access:  write_only
        .address_space:  global
        .offset:         32
        .size:           8
        .value_kind:     global_buffer
    .group_segment_fixed_size: 0
    .kernarg_segment_align: 8
    .kernarg_segment_size: 40
    .language:       OpenCL C
    .language_version:
      - 2
      - 0
    .max_flat_workgroup_size: 256
    .name:           _Z6k_prepPKfS0_P6__halfS2_Pi
    .private_segment_fixed_size: 0
    .sgpr_count:     18
    .sgpr_spill_count: 0
    .symbol:         _Z6k_prepPKfS0_P6__halfS2_Pi.kd
    .uniform_work_group_size: 1
    .uses_dynamic_stack: false
    .vgpr_count:     6
    .vgpr_spill_count: 0
    .wavefront_size: 64
  - .agpr_count:     0
    .args:
      - .actual_access:  read_only
        .address_space:  global
        .offset:         0
        .size:           8
        .value_kind:     global_buffer
      - .actual_access:  read_only
        .address_space:  global
        .offset:         8
        .size:           8
        .value_kind:     global_buffer
      - .address_space:  global
        .offset:         16
        .size:           8
        .value_kind:     global_buffer
      - .actual_access:  write_only
        .address_space:  global
        .offset:         24
        .size:           8
        .value_kind:     global_buffer
      - .actual_access:  write_only
        .address_space:  global
        .offset:         32
        .size:           8
        .value_kind:     global_buffer
      - .actual_access:  read_only
        .address_space:  global
        .offset:         40
        .size:           8
        .value_kind:     global_buffer
      - .actual_access:  read_only
        .address_space:  global
        .offset:         48
        .size:           8
        .value_kind:     global_buffer
      - .actual_access:  read_only
        .address_space:  global
        .offset:         56
        .size:           8
        .value_kind:     global_buffer
      - .actual_access:  read_only
        .address_space:  global
        .offset:         64
        .size:           8
        .value_kind:     global_buffer
      - .actual_access:  write_only
        .address_space:  global
        .offset:         72
        .size:           8
        .value_kind:     global_buffer
      - .actual_access:  read_only
        .address_space:  global
        .offset:         80
        .size:           8
        .value_kind:     global_buffer
      - .actual_access:  write_only
        .address_space:  global
        .offset:         88
        .size:           8
        .value_kind:     global_buffer
    .group_segment_fixed_size: 53248
    .kernarg_segment_align: 8
    .kernarg_segment_size: 96
    .language:       OpenCL C
    .language_version:
      - 2
      - 0
    .max_flat_workgroup_size: 256
    .name:           _Z15k_scatter_gemm1PKiS0_PiPjPyPKfPK6__halfS5_S5_PS6_PfSA_
    .private_segment_fixed_size: 0
    .sgpr_count:     32
    .sgpr_spill_count: 0
    .symbol:         _Z15k_scatter_gemm1PKiS0_PiPjPyPKfPK6__halfS5_S5_PS6_PfSA_.kd
    .uniform_work_group_size: 1
    .uses_dynamic_stack: false
    .vgpr_count:     162
    .vgpr_spill_count: 0
    .wavefront_size: 64
  - .agpr_count:     0
    .args:
      - .actual_access:  read_only
        .address_space:  global
        .offset:         0
        .size:           8
        .value_kind:     global_buffer
      - .actual_access:  read_only
        .address_space:  global
        .offset:         8
        .size:           8
        .value_kind:     global_buffer
      - .actual_access:  read_only
        .address_space:  global
        .offset:         16
        .size:           8
        .value_kind:     global_buffer
      - .actual_access:  write_only
        .address_space:  global
        .offset:         24
        .size:           8
        .value_kind:     global_buffer
      - .actual_access:  write_only
        .address_space:  global
        .offset:         32
        .size:           8
        .value_kind:     global_buffer
      - .actual_access:  write_only
        .address_space:  global
        .offset:         40
        .size:           8
        .value_kind:     global_buffer
      - .actual_access:  write_only
        .address_space:  global
        .offset:         48
        .size:           8
        .value_kind:     global_buffer
      - .actual_access:  read_only
        .address_space:  global
        .offset:         56
        .size:           8
        .value_kind:     global_buffer
      - .actual_access:  read_only
        .address_space:  global
        .offset:         64
        .size:           8
        .value_kind:     global_buffer
      - .actual_access:  read_only
        .address_space:  global
        .offset:         72
        .size:           8
        .value_kind:     global_buffer
      - .actual_access:  read_only
        .address_space:  global
        .offset:         80
        .size:           8
        .value_kind:     global_buffer
      - .actual_access:  write_only
        .address_space:  global
        .offset:         88
        .size:           8
        .value_kind:     global_buffer
      - .actual_access:  read_only
        .address_space:  global
        .offset:         96
        .size:           8
        .value_kind:     global_buffer
      - .actual_access:  write_only
        .address_space:  global
        .offset:         104
        .size:           8
        .value_kind:     global_buffer
    .group_segment_fixed_size: 53248
    .kernarg_segment_align: 8
    .kernarg_segment_size: 112
    .language:       OpenCL C
    .language_version:
      - 2
      - 0
    .max_flat_workgroup_size: 256
    .name:           _Z12k_fine_gemm1PKjPKyPKiPiS5_S5_S5_PKfPK6__halfS7_S7_PS8_PfSC_
    .private_segment_fixed_size: 0
    .sgpr_count:     102
    .sgpr_spill_count: 0
    .symbol:         _Z12k_fine_gemm1PKjPKyPKiPiS5_S5_S5_PKfPK6__halfS7_S7_PS8_PfSC_.kd
    .uniform_work_group_size: 1
    .uses_dynamic_stack: false
    .vgpr_count:     144
    .vgpr_spill_count: 0
    .wavefront_size: 64
  - .agpr_count:     0
    .args:
      - .actual_access:  read_only
        .address_space:  global
        .offset:         0
        .size:           8
        .value_kind:     global_buffer
      - .actual_access:  read_only
        .address_space:  global
        .offset:         8
        .size:           8
        .value_kind:     global_buffer
      - .actual_access:  read_only
        .address_space:  global
        .offset:         16
        .size:           8
        .value_kind:     global_buffer
      - .actual_access:  read_only
        .address_space:  global
        .offset:         24
        .size:           8
        .value_kind:     global_buffer
      - .actual_access:  read_only
        .address_space:  global
        .offset:         32
        .size:           8
        .value_kind:     global_buffer
      - .actual_access:  read_only
        .address_space:  global
        .offset:         40
        .size:           8
        .value_kind:     global_buffer
      - .actual_access:  read_only
        .address_space:  global
        .offset:         48
        .size:           8
        .value_kind:     global_buffer
      - .actual_access:  read_only
        .address_space:  global
        .offset:         56
        .size:           8
        .value_kind:     global_buffer
      - .actual_access:  read_only
        .address_space:  global
        .offset:         64
        .size:           8
        .value_kind:     global_buffer
      - .actual_access:  write_only
        .address_space:  global
        .offset:         72
        .size:           8
        .value_kind:     global_buffer
      - .actual_access:  read_only
        .address_space:  global
        .offset:         80
        .size:           8
        .value_kind:     global_buffer
      - .actual_access:  write_only
        .address_space:  global
        .offset:         88
        .size:           8
        .value_kind:     global_buffer
      - .actual_access:  read_only
        .address_space:  global
        .offset:         96
        .size:           8
        .value_kind:     global_buffer
      - .actual_access:  read_only
        .address_space:  global
        .offset:         104
        .size:           8
        .value_kind:     global_buffer
      - .actual_access:  read_only
        .address_space:  global
        .offset:         112
        .size:           8
        .value_kind:     global_buffer
    .group_segment_fixed_size: 5376
    .kernarg_segment_align: 8
    .kernarg_segment_size: 120
    .language:       OpenCL C
    .language_version:
      - 2
      - 0
    .max_flat_workgroup_size: 256
    .name:           _Z6k_agg1PKiS0_PK6__halfPKfS5_S5_S3_S5_S5_PS1_PfS7_S5_S0_S0_
    .private_segment_fixed_size: 0
    .sgpr_count:     43
    .sgpr_spill_count: 0
    .symbol:         _Z6k_agg1PKiS0_PK6__halfPKfS5_S5_S3_S5_S5_PS1_PfS7_S5_S0_S0_.kd
    .uniform_work_group_size: 1
    .uses_dynamic_stack: false
    .vgpr_count:     77
    .vgpr_spill_count: 0
    .wavefront_size: 64
  - .agpr_count:     0
    .args:
      - .actual_access:  read_only
        .address_space:  global
        .offset:         0
        .size:           8
        .value_kind:     global_buffer
      - .actual_access:  read_only
        .address_space:  global
        .offset:         8
        .size:           8
        .value_kind:     global_buffer
      - .actual_access:  read_only
        .address_space:  global
        .offset:         16
        .size:           8
        .value_kind:     global_buffer
      - .actual_access:  read_only
        .address_space:  global
        .offset:         24
        .size:           8
        .value_kind:     global_buffer
      - .actual_access:  read_only
        .address_space:  global
        .offset:         32
        .size:           8
        .value_kind:     global_buffer
      - .actual_access:  read_only
        .address_space:  global
        .offset:         40
        .size:           8
        .value_kind:     global_buffer
      - .actual_access:  write_only
        .address_space:  global
        .offset:         48
        .size:           8
        .value_kind:     global_buffer
      - .actual_access:  read_only
        .address_space:  global
        .offset:         56
        .size:           8
        .value_kind:     global_buffer
      - .actual_access:  read_only
        .address_space:  global
        .offset:         64
        .size:           8
        .value_kind:     global_buffer
      - .actual_access:  read_only
        .address_space:  global
        .offset:         72
        .size:           8
        .value_kind:     global_buffer
    .group_segment_fixed_size: 1024
    .kernarg_segment_align: 8
    .kernarg_segment_size: 80
    .language:       OpenCL C
    .language_version:
      - 2
      - 0
    .max_flat_workgroup_size: 256
    .name:           _Z6k_agg2PKiS0_PK6__halfPKfS5_S5_PfS5_S0_S0_
    .private_segment_fixed_size: 0
    .sgpr_count:     28
    .sgpr_spill_count: 0
    .symbol:         _Z6k_agg2PKiS0_PK6__halfPKfS5_S5_PfS5_S0_S0_.kd
    .uniform_work_group_size: 1
    .uses_dynamic_stack: false
    .vgpr_count:     60
    .vgpr_spill_count: 0
    .wavefront_size: 64
